# first-iteration peel with C=0 MFMAs and no accumulator clears also in the in-projection and down GEMM phases
# speedup vs baseline: 1.0048x; 1.0048x over previous
.LBB0_137:
	s_ashr_i32 s61, s60, 31
	s_lshl_b64 s[12:13], s[60:61], 18
	s_add_u32 s64, s76, s12
	s_addc_u32 s65, s77, s13
	s_and_b64 s[12:13], s[38:39], exec
	s_cselect_b32 s7, s65, s5
	s_cselect_b32 s10, s64, s4
	s_ashr_i32 s63, s62, 31
	s_lshl_b64 s[12:13], s[62:63], 18
	s_add_u32 s66, s78, s12
	s_addc_u32 s67, s79, s13
	s_and_b64 s[12:13], s[38:39], exec
	s_cselect_b32 s12, s67, s1
	s_cselect_b32 s13, s66, s0
	s_add_u32 s70, s4, 0x20080
	s_addc_u32 s71, s5, 0
	s_add_u32 s4, s0, 0x100
	s_addc_u32 s5, s1, 0
	s_mov_b32 s14, -2
	s_add_u32 s0, s70, 0xfffe0080
	s_addc_u32 s1, s71, -1
	s_add_i32 s16, 0, 0x10000
	s_cmp_eq_u32 s14, 4
	s_cselect_b32 s73, s7, s1
	s_cselect_b32 s72, s10, s0
	s_cselect_b32 s1, s12, s5
	s_cselect_b32 s0, s13, s4
	s_add_i32 s18, 0, 0x14000
	v_add_u32_e32 v0, s16, v182
	v_add_u32_e32 v4, s18, v182
	ds_read_b128 v[24:27], v0
	ds_read_b128 v[28:31], v0 offset:1024
	ds_read_b128 v[16:19], v0 offset:2048
	ds_read_b128 v[20:23], v0 offset:3072
	ds_read_b128 v[8:11], v4
	ds_read_b128 v[12:15], v4 offset:1024
	ds_read_b128 v[0:3], v4 offset:2048
	ds_read_b128 v[4:7], v4 offset:3072
	v_lshl_add_u64 v[196:197], s[70:71], 0, v[170:171]
	s_add_i32 m0, s93, 0xc000
	ds_read_b128 v[174:177], v186
	ds_read_b128 v[178:181], v186 offset:1024
	ds_read_b128 v[188:191], v186 offset:2048
	ds_read_b128 v[192:195], v186 offset:3072
	ds_read_b128 v[206:209], v186 offset:4096
	ds_read_b128 v[210:213], v186 offset:5120
	ds_read_b128 v[214:217], v186 offset:6144
	ds_read_b128 v[218:221], v186 offset:7168
	global_load_lds_dwordx4 v[196:197], off
	v_lshl_add_u64 v[196:197], s[70:71], 0, v[172:173]
	s_add_i32 m0, s93, 0xe000
	s_nop 0
	global_load_lds_dwordx4 v[196:197], off
	s_waitcnt vmcnt(8)
	s_waitcnt lgkmcnt(0)
	s_barrier
	s_setprio 1
	s_waitcnt lgkmcnt(0)
	v_mfma_f32_16x16x128_f8f6f4 v[158:161], v[24:31], v[174:181], 0
	v_mfma_f32_16x16x128_f8f6f4 v[154:157], v[16:23], v[174:181], 0
	v_mfma_f32_16x16x128_f8f6f4 v[142:145], v[24:31], v[188:195], 0
	v_mfma_f32_16x16x128_f8f6f4 v[138:141], v[16:23], v[188:195], 0
	v_mfma_f32_16x16x128_f8f6f4 v[126:129], v[24:31], v[206:213], 0
	v_mfma_f32_16x16x128_f8f6f4 v[122:125], v[16:23], v[206:213], 0
	v_mfma_f32_16x16x128_f8f6f4 v[110:113], v[24:31], v[214:221], 0
	v_mfma_f32_16x16x128_f8f6f4 v[106:109], v[16:23], v[214:221], 0
	s_setprio 0
	s_setprio 1
	v_mfma_f32_16x16x128_f8f6f4 v[150:153], v[8:15], v[174:181], 0
	v_mfma_f32_16x16x128_f8f6f4 v[146:149], v[0:7], v[174:181], 0
	v_mfma_f32_16x16x128_f8f6f4 v[134:137], v[8:15], v[188:195], 0
	v_mfma_f32_16x16x128_f8f6f4 v[130:133], v[0:7], v[188:195], 0
	v_mfma_f32_16x16x128_f8f6f4 v[118:121], v[8:15], v[206:213], 0
	v_mfma_f32_16x16x128_f8f6f4 v[114:117], v[0:7], v[206:213], 0
	v_mfma_f32_16x16x128_f8f6f4 v[102:105], v[8:15], v[214:221], 0
	v_mfma_f32_16x16x128_f8f6f4 v[98:101], v[0:7], v[214:221], 0
	s_setprio 0
	s_barrier
	s_add_i32 s16, s16, s80
	v_lshl_add_u64 v[174:175], s[0:1], 0, v[166:167]
	s_mov_b32 m0, s16
	ds_read_b128 v[188:191], v186 offset:16384
	ds_read_b128 v[192:195], v186 offset:17408
	ds_read_b128 v[206:209], v186 offset:18432
	ds_read_b128 v[210:213], v186 offset:19456
	ds_read_b128 v[214:217], v186 offset:20480
	ds_read_b128 v[218:221], v186 offset:21504
	ds_read_b128 v[240:243], v186 offset:22528
	ds_read_b128 v[244:247], v186 offset:23552
	global_load_lds_dwordx4 v[174:175], off
	s_add_i32 m0, s16, 0x2000
	s_add_u32 s20, s0, 0x8000
	v_lshl_add_u64 v[176:177], s[0:1], 0, v[162:163]
	s_addc_u32 s21, s1, 0
	s_add_i32 s16, s18, s80
	global_load_lds_dwordx4 v[176:177], off
	v_lshl_add_u64 v[178:179], s[20:21], 0, v[166:167]
	s_mov_b32 m0, s16
	v_lshl_add_u64 v[180:181], s[72:73], 0, v[164:165]
	global_load_lds_dwordx4 v[178:179], off
	v_lshl_add_u64 v[178:179], s[20:21], 0, v[162:163]
	s_add_i32 m0, s16, 0x2000
	s_nop 0
	global_load_lds_dwordx4 v[178:179], off
	v_lshl_add_u64 v[178:179], s[72:73], 0, v[168:169]
	s_mov_b32 m0, s93
	s_nop 0
	global_load_lds_dwordx4 v[178:179], off
	s_mov_b32 m0, s94
	s_nop 0
	global_load_lds_dwordx4 v[180:181], off
	s_waitcnt vmcnt(8)
	s_waitcnt lgkmcnt(0)
	s_barrier
	s_setprio 1
	s_waitcnt lgkmcnt(0)
	v_mfma_f32_16x16x128_f8f6f4 v[94:97], v[24:31], v[188:195], 0
	v_mfma_f32_16x16x128_f8f6f4 v[90:93], v[16:23], v[188:195], 0
	v_mfma_f32_16x16x128_f8f6f4 v[70:73], v[24:31], v[206:213], 0
	v_mfma_f32_16x16x128_f8f6f4 v[66:69], v[16:23], v[206:213], 0
	v_mfma_f32_16x16x128_f8f6f4 v[44:47], v[24:31], v[214:221], 0
	v_mfma_f32_16x16x128_f8f6f4 v[40:43], v[16:23], v[214:221], 0
	v_mfma_f32_16x16x128_f8f6f4 v[36:39], v[24:31], v[240:247], 0
	v_mfma_f32_16x16x128_f8f6f4 v[32:35], v[16:23], v[240:247], 0
	s_setprio 0
	s_setprio 1
	v_mfma_f32_16x16x128_f8f6f4 v[86:89], v[8:15], v[188:195], 0
	v_mfma_f32_16x16x128_f8f6f4 v[82:85], v[0:7], v[188:195], 0
	v_mfma_f32_16x16x128_f8f6f4 v[62:65], v[8:15], v[206:213], 0
	v_mfma_f32_16x16x128_f8f6f4 v[50:53], v[0:7], v[206:213], 0
	v_mfma_f32_16x16x128_f8f6f4 v[78:81], v[8:15], v[214:221], 0
	v_mfma_f32_16x16x128_f8f6f4 v[74:77], v[0:7], v[214:221], 0
	v_mfma_f32_16x16x128_f8f6f4 v[58:61], v[8:15], v[240:247], 0
	v_mfma_f32_16x16x128_f8f6f4 v[54:57], v[0:7], v[240:247], 0
	s_setprio 0
	s_barrier
	s_add_i32 s16, 0, 0x18000
	s_add_i32 s20, 0, 0x1c000
	v_add_u32_e32 v12, s16, v182
	v_add_u32_e32 v28, s20, v182
	ds_read_b128 v[0:3], v12
	ds_read_b128 v[4:7], v12 offset:1024
	ds_read_b128 v[8:11], v12 offset:2048
	ds_read_b128 v[12:15], v12 offset:3072
	ds_read_b128 v[16:19], v28
	ds_read_b128 v[20:23], v28 offset:1024
	ds_read_b128 v[24:27], v28 offset:2048
	ds_read_b128 v[28:31], v28 offset:3072
	s_add_u32 s18, s72, 0x20000
	s_addc_u32 s19, s73, 0
	s_mov_b32 m0, s95
	v_lshl_add_u64 v[196:197], s[18:19], 0, v[168:169]
	ds_read_b128 v[188:191], v186 offset:32768
	ds_read_b128 v[192:195], v186 offset:33792
	ds_read_b128 v[206:209], v186 offset:34816
	ds_read_b128 v[210:213], v186 offset:35840
	ds_read_b128 v[214:217], v186 offset:36864
	ds_read_b128 v[218:221], v186 offset:37888
	ds_read_b128 v[240:243], v186 offset:38912
	ds_read_b128 v[244:247], v186 offset:39936
	global_load_lds_dwordx4 v[196:197], off
	v_lshl_add_u64 v[196:197], s[18:19], 0, v[164:165]
	s_mov_b32 m0, s96
	s_nop 0
	global_load_lds_dwordx4 v[196:197], off
	s_waitcnt vmcnt(8)
	s_waitcnt lgkmcnt(0)
	s_barrier
	s_setprio 1
	s_waitcnt lgkmcnt(0)
	v_mfma_f32_16x16x128_f8f6f4 v[158:161], v[0:7], v[188:195], v[158:161]
	v_mfma_f32_16x16x128_f8f6f4 v[154:157], v[8:15], v[188:195], v[154:157]
	v_mfma_f32_16x16x128_f8f6f4 v[142:145], v[0:7], v[206:213], v[142:145]
	v_mfma_f32_16x16x128_f8f6f4 v[138:141], v[8:15], v[206:213], v[138:141]
	v_mfma_f32_16x16x128_f8f6f4 v[126:129], v[0:7], v[214:221], v[126:129]
	v_mfma_f32_16x16x128_f8f6f4 v[122:125], v[8:15], v[214:221], v[122:125]
	v_mfma_f32_16x16x128_f8f6f4 v[110:113], v[0:7], v[240:247], v[110:113]
	v_mfma_f32_16x16x128_f8f6f4 v[106:109], v[8:15], v[240:247], v[106:109]
	s_setprio 0
	s_setprio 1
	v_mfma_f32_16x16x128_f8f6f4 v[150:153], v[16:23], v[188:195], v[150:153]
	v_mfma_f32_16x16x128_f8f6f4 v[146:149], v[24:31], v[188:195], v[146:149]
	v_mfma_f32_16x16x128_f8f6f4 v[134:137], v[16:23], v[206:213], v[134:137]
	v_mfma_f32_16x16x128_f8f6f4 v[130:133], v[24:31], v[206:213], v[130:133]
	v_mfma_f32_16x16x128_f8f6f4 v[118:121], v[16:23], v[214:221], v[118:121]
	v_mfma_f32_16x16x128_f8f6f4 v[114:117], v[24:31], v[214:221], v[114:117]
	v_mfma_f32_16x16x128_f8f6f4 v[102:105], v[16:23], v[240:247], v[102:105]
	v_mfma_f32_16x16x128_f8f6f4 v[98:101], v[24:31], v[240:247], v[98:101]
	s_setprio 0
	s_barrier
	s_add_i32 s16, s16, s80
	v_lshl_add_u64 v[174:175], v[174:175], 0, s[88:89]
	s_mov_b32 m0, s16
	ds_read_b128 v[188:191], v186 offset:49152
	ds_read_b128 v[192:195], v186 offset:50176
	ds_read_b128 v[206:209], v186 offset:51200
	ds_read_b128 v[210:213], v186 offset:52224
	ds_read_b128 v[214:217], v186 offset:53248
	ds_read_b128 v[218:221], v186 offset:54272
	ds_read_b128 v[240:243], v186 offset:55296
	ds_read_b128 v[244:247], v186 offset:56320
	global_load_lds_dwordx4 v[174:175], off
	s_add_i32 m0, s16, 0x2000
	s_add_u32 s0, s0, 0x8080
	v_lshl_add_u64 v[174:175], v[176:177], 0, s[88:89]
	s_addc_u32 s1, s1, 0
	s_add_i32 s16, s20, s80
	global_load_lds_dwordx4 v[174:175], off
	v_lshl_add_u64 v[174:175], s[0:1], 0, v[166:167]
	s_mov_b32 m0, s16
	s_nop 0
	global_load_lds_dwordx4 v[174:175], off
	v_lshl_add_u64 v[174:175], s[0:1], 0, v[162:163]
	s_add_i32 m0, s16, 0x2000
	s_nop 0
	global_load_lds_dwordx4 v[174:175], off
	v_lshl_add_u64 v[174:175], v[178:179], 0, s[88:89]
	s_mov_b32 m0, s9
	s_nop 0
	global_load_lds_dwordx4 v[174:175], off
	v_lshl_add_u64 v[174:175], v[180:181], 0, s[88:89]
	s_mov_b32 m0, s97
	s_nop 0
	global_load_lds_dwordx4 v[174:175], off
	s_waitcnt vmcnt(8)
	s_waitcnt lgkmcnt(0)
	s_barrier
	s_setprio 1
	s_waitcnt lgkmcnt(0)
	v_mfma_f32_16x16x128_f8f6f4 v[94:97], v[0:7], v[188:195], v[94:97]
	v_mfma_f32_16x16x128_f8f6f4 v[90:93], v[8:15], v[188:195], v[90:93]
	v_mfma_f32_16x16x128_f8f6f4 v[70:73], v[0:7], v[206:213], v[70:73]
	v_mfma_f32_16x16x128_f8f6f4 v[66:69], v[8:15], v[206:213], v[66:69]
	v_mfma_f32_16x16x128_f8f6f4 v[44:47], v[0:7], v[214:221], v[44:47]
	v_mfma_f32_16x16x128_f8f6f4 v[40:43], v[8:15], v[214:221], v[40:43]
	v_mfma_f32_16x16x128_f8f6f4 v[36:39], v[0:7], v[240:247], v[36:39]
	v_mfma_f32_16x16x128_f8f6f4 v[32:35], v[8:15], v[240:247], v[32:35]
	s_setprio 0
	s_setprio 1
	v_mfma_f32_16x16x128_f8f6f4 v[86:89], v[16:23], v[188:195], v[86:89]
	v_mfma_f32_16x16x128_f8f6f4 v[82:85], v[24:31], v[188:195], v[82:85]
	v_mfma_f32_16x16x128_f8f6f4 v[62:65], v[16:23], v[206:213], v[62:65]
	v_mfma_f32_16x16x128_f8f6f4 v[50:53], v[24:31], v[206:213], v[50:53]
	v_mfma_f32_16x16x128_f8f6f4 v[78:81], v[16:23], v[214:221], v[78:81]
	v_mfma_f32_16x16x128_f8f6f4 v[74:77], v[24:31], v[214:221], v[74:77]
	v_mfma_f32_16x16x128_f8f6f4 v[58:61], v[16:23], v[240:247], v[58:61]
	v_mfma_f32_16x16x128_f8f6f4 v[54:57], v[24:31], v[240:247], v[54:57]
	s_setprio 0
	s_barrier
	s_add_i32 s14, s14, 2
	s_add_u32 s70, s70, 0x100
	s_addc_u32 s71, s71, 0
	s_add_u32 s4, s4, 0x100
	s_addc_u32 s5, s5, 0
	s_cmp_gt_u32 s14, 5

.LBB0_986:
	s_ashr_i32 s45, s44, 31
	s_lshl_b64 s[30:31], s[44:45], 18
	s_add_u32 s48, s7, s30
	s_addc_u32 s49, s8, s31
	s_and_b64 s[30:31], s[36:37], exec
	s_cselect_b32 s21, s49, s5
	s_cselect_b32 s30, s48, s4
	s_ashr_i32 s47, s46, 31
	s_lshl_b64 s[50:51], s[46:47], 18
	s_add_u32 s50, s9, s50
	s_addc_u32 s51, s10, s51
	s_and_b64 s[56:57], s[36:37], exec
	s_cselect_b32 s31, s51, s1
	s_cselect_b32 s33, s50, s0
	s_add_u32 s56, s4, 0x20080
	s_addc_u32 s57, s5, 0
	s_add_u32 s4, s0, 0x100
	s_addc_u32 s5, s1, 0
	s_mov_b32 s45, -2
	s_add_u32 s0, s56, 0xfffe0080
	s_addc_u32 s1, s57, -1
	s_add_i32 s47, 0, 0x10000
	s_cmp_eq_u32 s45, 4
	s_cselect_b32 s59, s21, s1
	s_cselect_b32 s58, s30, s0
	s_cselect_b32 s1, s31, s5
	s_cselect_b32 s0, s33, s4
	s_add_i32 s53, 0, 0x14000
	v_add_u32_e32 v0, s47, v182
	v_add_u32_e32 v4, s53, v182
	ds_read_b128 v[24:27], v0
	ds_read_b128 v[28:31], v0 offset:1024
	ds_read_b128 v[16:19], v0 offset:2048
	ds_read_b128 v[20:23], v0 offset:3072
	ds_read_b128 v[8:11], v4
	ds_read_b128 v[12:15], v4 offset:1024
	ds_read_b128 v[0:3], v4 offset:2048
	ds_read_b128 v[4:7], v4 offset:3072
	v_lshl_add_u64 v[212:213], s[56:57], 0, v[170:171]
	s_add_i32 m0, s12, 0xc000
	ds_read_b128 v[174:177], v186
	ds_read_b128 v[178:181], v186 offset:1024
	ds_read_b128 v[188:191], v186 offset:2048
	ds_read_b128 v[192:195], v186 offset:3072
	ds_read_b128 v[196:199], v186 offset:4096
	ds_read_b128 v[200:203], v186 offset:5120
	ds_read_b128 v[204:207], v186 offset:6144
	ds_read_b128 v[208:211], v186 offset:7168
	global_load_lds_dwordx4 v[212:213], off
	v_lshl_add_u64 v[212:213], s[56:57], 0, v[172:173]
	s_add_i32 m0, s12, 0xe000
	s_nop 0
	global_load_lds_dwordx4 v[212:213], off
	s_waitcnt vmcnt(8)
	s_waitcnt lgkmcnt(0)
	s_barrier
	s_setprio 1
	s_waitcnt lgkmcnt(0)
	v_mfma_f32_16x16x128_f8f6f4 v[158:161], v[24:31], v[174:181], 0
	v_mfma_f32_16x16x128_f8f6f4 v[154:157], v[16:23], v[174:181], 0
	v_mfma_f32_16x16x128_f8f6f4 v[142:145], v[24:31], v[188:195], 0
	v_mfma_f32_16x16x128_f8f6f4 v[138:141], v[16:23], v[188:195], 0
	v_mfma_f32_16x16x128_f8f6f4 v[126:129], v[24:31], v[196:203], 0
	v_mfma_f32_16x16x128_f8f6f4 v[122:125], v[16:23], v[196:203], 0
	v_mfma_f32_16x16x128_f8f6f4 v[110:113], v[24:31], v[204:211], 0
	v_mfma_f32_16x16x128_f8f6f4 v[106:109], v[16:23], v[204:211], 0
	s_setprio 0
	s_setprio 1
	v_mfma_f32_16x16x128_f8f6f4 v[150:153], v[8:15], v[174:181], 0
	v_mfma_f32_16x16x128_f8f6f4 v[146:149], v[0:7], v[174:181], 0
	v_mfma_f32_16x16x128_f8f6f4 v[134:137], v[8:15], v[188:195], 0
	v_mfma_f32_16x16x128_f8f6f4 v[130:133], v[0:7], v[188:195], 0
	v_mfma_f32_16x16x128_f8f6f4 v[118:121], v[8:15], v[196:203], 0
	v_mfma_f32_16x16x128_f8f6f4 v[114:117], v[0:7], v[196:203], 0
	v_mfma_f32_16x16x128_f8f6f4 v[102:105], v[8:15], v[204:211], 0
	v_mfma_f32_16x16x128_f8f6f4 v[98:101], v[0:7], v[204:211], 0
	s_setprio 0
	s_barrier
	s_add_i32 s47, s47, s6
	v_lshl_add_u64 v[174:175], s[0:1], 0, v[164:165]
	s_mov_b32 m0, s47
	ds_read_b128 v[188:191], v186 offset:16384
	ds_read_b128 v[192:195], v186 offset:17408
	ds_read_b128 v[196:199], v186 offset:18432
	ds_read_b128 v[200:203], v186 offset:19456
	ds_read_b128 v[204:207], v186 offset:20480
	ds_read_b128 v[208:211], v186 offset:21504
	ds_read_b128 v[212:215], v186 offset:22528
	ds_read_b128 v[216:219], v186 offset:23552
	global_load_lds_dwordx4 v[174:175], off
	s_add_i32 m0, s47, 0x2000
	s_add_u32 s60, s0, 0x8000
	v_lshl_add_u64 v[176:177], s[0:1], 0, v[168:169]
	s_addc_u32 s61, s1, 0
	s_add_i32 s47, s53, s6
	global_load_lds_dwordx4 v[176:177], off
	v_lshl_add_u64 v[178:179], s[60:61], 0, v[164:165]
	s_mov_b32 m0, s47
	v_lshl_add_u64 v[180:181], s[58:59], 0, v[166:167]
	global_load_lds_dwordx4 v[178:179], off
	v_lshl_add_u64 v[178:179], s[60:61], 0, v[168:169]
	s_add_i32 m0, s47, 0x2000
	s_nop 0
	global_load_lds_dwordx4 v[178:179], off
	v_lshl_add_u64 v[178:179], s[58:59], 0, v[162:163]
	s_mov_b32 m0, s12
	s_nop 0
	global_load_lds_dwordx4 v[178:179], off
	s_mov_b32 m0, s13
	s_nop 0
	global_load_lds_dwordx4 v[180:181], off
	s_waitcnt vmcnt(8)
	s_waitcnt lgkmcnt(0)
	s_barrier
	s_setprio 1
	s_waitcnt lgkmcnt(0)
	v_mfma_f32_16x16x128_f8f6f4 v[94:97], v[24:31], v[188:195], 0
	v_mfma_f32_16x16x128_f8f6f4 v[90:93], v[16:23], v[188:195], 0
	v_mfma_f32_16x16x128_f8f6f4 v[78:81], v[24:31], v[196:203], 0
	v_mfma_f32_16x16x128_f8f6f4 v[74:77], v[16:23], v[196:203], 0
	v_mfma_f32_16x16x128_f8f6f4 v[58:61], v[24:31], v[204:211], 0
	v_mfma_f32_16x16x128_f8f6f4 v[50:53], v[16:23], v[204:211], 0
	v_mfma_f32_16x16x128_f8f6f4 v[40:43], v[24:31], v[212:219], 0
	v_mfma_f32_16x16x128_f8f6f4 v[32:35], v[16:23], v[212:219], 0
	s_setprio 0
	s_setprio 1
	v_mfma_f32_16x16x128_f8f6f4 v[86:89], v[8:15], v[188:195], 0
	v_mfma_f32_16x16x128_f8f6f4 v[82:85], v[0:7], v[188:195], 0
	v_mfma_f32_16x16x128_f8f6f4 v[70:73], v[8:15], v[196:203], 0
	v_mfma_f32_16x16x128_f8f6f4 v[66:69], v[0:7], v[196:203], 0
	v_mfma_f32_16x16x128_f8f6f4 v[62:65], v[8:15], v[204:211], 0
	v_mfma_f32_16x16x128_f8f6f4 v[54:57], v[0:7], v[204:211], 0
	v_mfma_f32_16x16x128_f8f6f4 v[44:47], v[8:15], v[212:219], 0
	v_mfma_f32_16x16x128_f8f6f4 v[36:39], v[0:7], v[212:219], 0
	s_setprio 0
	s_barrier
	s_add_i32 s47, 0, 0x18000
	s_add_i32 s53, 0, 0x1c000
	v_add_u32_e32 v12, s47, v182
	v_add_u32_e32 v28, s53, v182
	ds_read_b128 v[0:3], v12
	ds_read_b128 v[4:7], v12 offset:1024
	ds_read_b128 v[8:11], v12 offset:2048
	ds_read_b128 v[12:15], v12 offset:3072
	ds_read_b128 v[16:19], v28
	ds_read_b128 v[20:23], v28 offset:1024
	ds_read_b128 v[24:27], v28 offset:2048
	ds_read_b128 v[28:31], v28 offset:3072
	s_add_u32 s58, s58, 0x20000
	s_addc_u32 s59, s59, 0
	s_mov_b32 m0, s14
	v_lshl_add_u64 v[220:221], s[58:59], 0, v[162:163]
	ds_read_b128 v[188:191], v186 offset:32768
	ds_read_b128 v[192:195], v186 offset:33792
	ds_read_b128 v[196:199], v186 offset:34816
	ds_read_b128 v[200:203], v186 offset:35840
	ds_read_b128 v[204:207], v186 offset:36864
	ds_read_b128 v[208:211], v186 offset:37888
	ds_read_b128 v[212:215], v186 offset:38912
	ds_read_b128 v[216:219], v186 offset:39936
	global_load_lds_dwordx4 v[220:221], off
	v_lshl_add_u64 v[220:221], s[58:59], 0, v[166:167]
	s_mov_b32 m0, s16
	s_nop 0
	global_load_lds_dwordx4 v[220:221], off
	s_waitcnt vmcnt(8)
	s_waitcnt lgkmcnt(0)
	s_barrier
	s_setprio 1
	s_waitcnt lgkmcnt(0)
	v_mfma_f32_16x16x128_f8f6f4 v[158:161], v[0:7], v[188:195], v[158:161]
	v_mfma_f32_16x16x128_f8f6f4 v[154:157], v[8:15], v[188:195], v[154:157]
	v_mfma_f32_16x16x128_f8f6f4 v[142:145], v[0:7], v[196:203], v[142:145]
	v_mfma_f32_16x16x128_f8f6f4 v[138:141], v[8:15], v[196:203], v[138:141]
	v_mfma_f32_16x16x128_f8f6f4 v[126:129], v[0:7], v[204:211], v[126:129]
	v_mfma_f32_16x16x128_f8f6f4 v[122:125], v[8:15], v[204:211], v[122:125]
	v_mfma_f32_16x16x128_f8f6f4 v[110:113], v[0:7], v[212:219], v[110:113]
	v_mfma_f32_16x16x128_f8f6f4 v[106:109], v[8:15], v[212:219], v[106:109]
	s_setprio 0
	s_setprio 1
	v_mfma_f32_16x16x128_f8f6f4 v[150:153], v[16:23], v[188:195], v[150:153]
	v_mfma_f32_16x16x128_f8f6f4 v[146:149], v[24:31], v[188:195], v[146:149]
	v_mfma_f32_16x16x128_f8f6f4 v[134:137], v[16:23], v[196:203], v[134:137]
	v_mfma_f32_16x16x128_f8f6f4 v[130:133], v[24:31], v[196:203], v[130:133]
	v_mfma_f32_16x16x128_f8f6f4 v[118:121], v[16:23], v[204:211], v[118:121]
	v_mfma_f32_16x16x128_f8f6f4 v[114:117], v[24:31], v[204:211], v[114:117]
	v_mfma_f32_16x16x128_f8f6f4 v[102:105], v[16:23], v[212:219], v[102:105]
	v_mfma_f32_16x16x128_f8f6f4 v[98:101], v[24:31], v[212:219], v[98:101]
	s_setprio 0
	s_barrier
	s_add_i32 s47, s47, s6
	v_lshl_add_u64 v[174:175], v[174:175], 0, s[88:89]
	s_mov_b32 m0, s47
	ds_read_b128 v[188:191], v186 offset:49152
	ds_read_b128 v[192:195], v186 offset:50176
	ds_read_b128 v[196:199], v186 offset:51200
	ds_read_b128 v[200:203], v186 offset:52224
	ds_read_b128 v[204:207], v186 offset:53248
	ds_read_b128 v[208:211], v186 offset:54272
	ds_read_b128 v[212:215], v186 offset:55296
	ds_read_b128 v[216:219], v186 offset:56320
	global_load_lds_dwordx4 v[174:175], off
	s_add_i32 m0, s47, 0x2000
	s_add_u32 s0, s0, 0x8080
	v_lshl_add_u64 v[174:175], v[176:177], 0, s[88:89]
	s_addc_u32 s1, s1, 0
	s_add_i32 s47, s53, s6
	global_load_lds_dwordx4 v[174:175], off
	v_lshl_add_u64 v[174:175], s[0:1], 0, v[164:165]
	s_mov_b32 m0, s47
	s_nop 0
	global_load_lds_dwordx4 v[174:175], off
	v_lshl_add_u64 v[174:175], s[0:1], 0, v[168:169]
	s_add_i32 m0, s47, 0x2000
	s_nop 0
	global_load_lds_dwordx4 v[174:175], off
	v_lshl_add_u64 v[174:175], v[178:179], 0, s[88:89]
	s_mov_b32 m0, s18
	s_nop 0
	global_load_lds_dwordx4 v[174:175], off
	v_lshl_add_u64 v[174:175], v[180:181], 0, s[88:89]
	s_mov_b32 m0, s19
	s_nop 0
	global_load_lds_dwordx4 v[174:175], off
	s_waitcnt vmcnt(8)
	s_waitcnt lgkmcnt(0)
	s_barrier
	s_setprio 1
	s_waitcnt lgkmcnt(0)
	v_mfma_f32_16x16x128_f8f6f4 v[94:97], v[0:7], v[188:195], v[94:97]
	v_mfma_f32_16x16x128_f8f6f4 v[90:93], v[8:15], v[188:195], v[90:93]
	v_mfma_f32_16x16x128_f8f6f4 v[78:81], v[0:7], v[196:203], v[78:81]
	v_mfma_f32_16x16x128_f8f6f4 v[74:77], v[8:15], v[196:203], v[74:77]
	v_mfma_f32_16x16x128_f8f6f4 v[58:61], v[0:7], v[204:211], v[58:61]
	v_mfma_f32_16x16x128_f8f6f4 v[50:53], v[8:15], v[204:211], v[50:53]
	v_mfma_f32_16x16x128_f8f6f4 v[40:43], v[0:7], v[212:219], v[40:43]
	v_mfma_f32_16x16x128_f8f6f4 v[32:35], v[8:15], v[212:219], v[32:35]
	s_setprio 0
	s_setprio 1
	v_mfma_f32_16x16x128_f8f6f4 v[86:89], v[16:23], v[188:195], v[86:89]
	v_mfma_f32_16x16x128_f8f6f4 v[82:85], v[24:31], v[188:195], v[82:85]
	v_mfma_f32_16x16x128_f8f6f4 v[70:73], v[16:23], v[196:203], v[70:73]
	v_mfma_f32_16x16x128_f8f6f4 v[66:69], v[24:31], v[196:203], v[66:69]
	v_mfma_f32_16x16x128_f8f6f4 v[62:65], v[16:23], v[204:211], v[62:65]
	v_mfma_f32_16x16x128_f8f6f4 v[54:57], v[24:31], v[204:211], v[54:57]
	v_mfma_f32_16x16x128_f8f6f4 v[44:47], v[16:23], v[212:219], v[44:47]
	v_mfma_f32_16x16x128_f8f6f4 v[36:39], v[24:31], v[212:219], v[36:39]
	s_setprio 0
	s_barrier
	s_add_i32 s45, s45, 2
	s_add_u32 s56, s56, 0x100
	s_addc_u32 s57, s57, 0
	s_add_u32 s4, s4, 0x100
	s_addc_u32 s5, s5, 0
	s_cmp_gt_u32 s45, 5
